# P9 LN2 tail: gamma/beta loads hoisted above the reductions, serialized load-wait-store ladder removed
# speedup vs baseline: 1.0240x; 1.0032x over previous
; #define GAS __attribute__((address_space(1)))
; __device__ __forceinline__ void p9_combine(Frame& F, const LAS int* tstart) {
;     ...
;         const float mean1 = st1[2 * m], rstd1 = st1[2 * m + 1];
;         size_t ro[4]; float gk[4];
; #pragma unroll
;         for (int k = 0; k < 4; ++k) { const int e = topi[4 * m + k]; ro[k] = ((size_t)tstart[e] * 256 + posb[4 * m + k]) * D; gk[k] = gate[4 * m + k]; }
;         f32x4 v[8]; float s = 0.f;
; #pragma unroll
;         for (int j = 0; j < 8; ++j) { const int col = 4 * lane + 256 * j;
;             const v2u zw = *(const GAS v2u*)(z1 + (size_t)m * D + col); const f32x4 zv = (f32x4){bf_lo(zw.x), bf_hi(zw.x), bf_lo(zw.y), bf_hi(zw.y)}, g = *(const GAS f32x4*)(F.ln1_g + col), b = *(const GAS f32x4*)(F.ln1_b + col);
;             f32x4 a = ((zv - mean1) * rstd1 * g + b) * ALPHA;
.LBB0_1798:
	s_ashr_i32 s7, s6, 31
	s_lshl_b64 s[0:1], s[6:7], 2
	s_add_u32 s0, s18, s0
	s_addc_u32 s1, s19, s1
	s_ashr_i32 s9, s8, 31
	global_load_dwordx2 v[118:119], v[116:117], off
	global_load_dwordx2 v[120:121], v[116:117], off offset:512
	global_load_dwordx4 v[0:3], v[74:75], off
	global_load_dwordx4 v[4:7], v[74:75], off offset:1024
	global_load_dwordx4 v[12:15], v[76:77], off
	global_load_dwordx4 v[8:11], v[76:77], off offset:1024
	global_load_dwordx2 v[122:123], v[116:117], off offset:1024
	global_load_dwordx2 v[124:125], v[116:117], off offset:1536
	global_load_dwordx4 v[16:19], v[74:75], off offset:2048
	global_load_dwordx4 v[20:23], v[74:75], off offset:3072
	global_load_dwordx4 v[28:31], v[76:77], off offset:2048
	global_load_dwordx4 v[24:27], v[76:77], off offset:3072
	global_load_dwordx4 v[32:35], v[78:79], off
	global_load_dwordx4 v[40:43], v[80:81], off
	global_load_dwordx2 v[126:127], v[116:117], off offset:2048
	global_load_dwordx2 v[128:129], v[116:117], off offset:2560
	global_load_dwordx4 v[48:51], v[82:83], off
	global_load_dwordx4 v[52:55], v[84:85], off
	global_load_dwordx4 v[56:59], v[86:87], off
	global_load_dwordx4 v[60:63], v[88:89], off
	global_load_dwordx2 v[130:131], v[116:117], off offset:3072
	global_load_dwordx2 v[132:133], v[116:117], off offset:3584
	global_load_dwordx4 v[64:67], v[90:91], off
	global_load_dwordx4 v[68:71], v[92:93], off
	global_load_dwordx4 v[36:39], v[94:95], off
	global_load_dwordx4 v[44:47], v[96:97], off
	global_load_dwordx2 v[152:153], v140, s[0:1]
	s_lshl_b64 s[0:1], s[8:9], 2
	s_add_u32 s26, s20, s0
	s_addc_u32 s27, s21, s1
	global_load_dwordx4 v[144:147], v140, s[26:27]
	s_add_u32 s26, s24, s0
	s_addc_u32 s27, s25, s1
	s_add_u32 s0, s22, s0
	s_addc_u32 s1, s23, s1
	global_load_dword v154, v140, s[26:27]
	global_load_dword v143, v140, s[0:1]
	s_add_i32 s26, s8, 1
	s_ashr_i32 s27, s26, 31
	s_lshl_b64 s[0:1], s[26:27], 2
	s_add_u32 s26, s24, s0
	s_addc_u32 s27, s25, s1
	global_load_dwordx3 v[148:150], v140, s[26:27]
	s_add_u32 s0, s22, s0
	s_addc_u32 s1, s23, s1
	global_load_dword v151, v140, s[0:1]
	s_add_i32 s26, s8, 2
	s_ashr_i32 s27, s26, 31
	s_lshl_b64 s[0:1], s[26:27], 2
	s_add_u32 s0, s22, s0
	s_addc_u32 s1, s23, s1
	global_load_dwordx2 v[156:157], v140, s[0:1]
	s_add_i32 s2, s2, s16
	s_add_i32 s6, s6, s13
	s_add_i32 s8, s8, s14
	v_lshl_add_u64 v[116:117], v[116:117], 0, s[10:11]
	s_cmpk_lt_i32 s2, 0x4000
	s_waitcnt vmcnt(31)
	v_lshlrev_b32_e32 v160, 16, v120
	v_and_b32_e32 v161, 0xffff0000, v120
	v_lshlrev_b32_e32 v162, 16, v121
	v_and_b32_e32 v163, 0xffff0000, v121
	s_waitcnt vmcnt(26)
	v_lshlrev_b32_e32 v164, 16, v122
	v_and_b32_e32 v165, 0xffff0000, v122
	v_lshlrev_b32_e32 v166, 16, v123
	v_and_b32_e32 v167, 0xffff0000, v123
	s_waitcnt vmcnt(25)
	v_lshlrev_b32_e32 v168, 16, v124
	v_and_b32_e32 v169, 0xffff0000, v124
	v_lshlrev_b32_e32 v170, 16, v125
	v_and_b32_e32 v171, 0xffff0000, v125
	s_waitcnt vmcnt(18)
	v_lshlrev_b32_e32 v172, 16, v126
	v_and_b32_e32 v173, 0xffff0000, v126
	v_lshlrev_b32_e32 v174, 16, v127
	v_and_b32_e32 v175, 0xffff0000, v127
	s_waitcnt vmcnt(17)
	v_lshlrev_b32_e32 v176, 16, v128
	v_and_b32_e32 v177, 0xffff0000, v128
	v_lshlrev_b32_e32 v178, 16, v129
	v_and_b32_e32 v179, 0xffff0000, v129
	s_waitcnt vmcnt(12)
	v_lshlrev_b32_e32 v180, 16, v130
	v_and_b32_e32 v181, 0xffff0000, v130
	v_lshlrev_b32_e32 v158, 16, v119
	v_and_b32_e32 v159, 0xffff0000, v119
	s_waitcnt vmcnt(6)
	v_sub_f32_e32 v121, v159, v152
	v_sub_f32_e32 v120, v158, v152
	v_sub_f32_e32 v123, v161, v152
	v_sub_f32_e32 v122, v160, v152
	v_sub_f32_e32 v125, v163, v152
	v_sub_f32_e32 v124, v162, v152
	v_sub_f32_e32 v127, v165, v152
	v_sub_f32_e32 v126, v164, v152
	v_sub_f32_e32 v129, v167, v152
	v_sub_f32_e32 v128, v166, v152
	v_sub_f32_e32 v159, v173, v152
	v_sub_f32_e32 v158, v172, v152
	v_sub_f32_e32 v161, v175, v152
	v_sub_f32_e32 v160, v174, v152
	v_pk_mul_f32 v[124:125], v[152:153], v[124:125] op_sel:[1,0]
	v_pk_mul_f32 v[122:123], v[152:153], v[122:123] op_sel:[1,0]
	v_pk_mul_f32 v[128:129], v[152:153], v[128:129] op_sel:[1,0]
	v_pk_mul_f32 v[126:127], v[152:153], v[126:127] op_sel:[1,0]
	v_pk_mul_f32 v[160:161], v[152:153], v[160:161] op_sel:[1,0]
	v_pk_mul_f32 v[158:159], v[152:153], v[158:159] op_sel:[1,0]
	v_pk_fma_f32 v[4:5], v[4:5], v[122:123], v[8:9]
	v_pk_fma_f32 v[6:7], v[6:7], v[124:125], v[10:11]
	v_pk_fma_f32 v[8:9], v[16:17], v[126:127], v[28:29]
	v_pk_fma_f32 v[10:11], v[18:19], v[128:129], v[30:31]
	v_pk_fma_f32 v[16:17], v[32:33], v[158:159], v[40:41]
	v_pk_fma_f32 v[18:19], v[34:35], v[160:161], v[42:43]
	s_waitcnt vmcnt(5)
	v_lshlrev_b32_e32 v32, 2, v144
	v_lshlrev_b32_e32 v34, 2, v146
	v_lshlrev_b32_e32 v33, 2, v145
	v_lshlrev_b32_e32 v35, 2, v147
	v_add_u32_e32 v32, s3, v32
	v_add_u32_e32 v40, s3, v34
	v_lshlrev_b32_e32 v155, 16, v118
	v_and_b32_e32 v118, 0xffff0000, v118
	v_add_u32_e32 v33, s3, v33
	v_add_u32_e32 v35, s3, v35
	ds_read_b32 v32, v32
	ds_read_b32 v34, v33
	ds_read_b32 v40, v40
	ds_read_b32 v42, v35
	v_lshlrev_b32_e32 v182, 16, v131
	v_and_b32_e32 v183, 0xffff0000, v131
	v_sub_f32_e32 v119, v118, v152
	v_sub_f32_e32 v118, v155, v152
	v_sub_f32_e32 v131, v169, v152
	v_sub_f32_e32 v130, v168, v152
	v_sub_f32_e32 v163, v177, v152
	v_sub_f32_e32 v162, v176, v152
	v_pk_mul_f32 v[118:119], v[152:153], v[118:119] op_sel:[1,0]
	v_pk_mul_f32 v[130:131], v[152:153], v[130:131] op_sel:[1,0]
	v_pk_mul_f32 v[162:163], v[152:153], v[162:163] op_sel:[1,0]
	s_waitcnt vmcnt(4)
	v_ashrrev_i32_e32 v155, 31, v154
	s_waitcnt lgkmcnt(3)
; #define GAS __attribute__((address_space(1)))
; __device__ __forceinline__ void p9_combine(Frame& F, const LAS int* tstart) {
;     ...
;         size_t ro[4]; float gk[4];
; #pragma unroll
;         for (int k = 0; k < 4; ++k) { const int e = topi[4 * m + k]; ro[k] = ((size_t)tstart[e] * 256 + posb[4 * m + k]) * D; gk[k] = gate[4 * m + k]; }
;         f32x4 v[8]; float s = 0.f;
; #pragma unroll
;         for (int j = 0; j < 8; ++j) { const int col = 4 * lane + 256 * j;
;             const v2u zw = *(const GAS v2u*)(z1 + (size_t)m * D + col); const f32x4 zv = (f32x4){bf_lo(zw.x), bf_hi(zw.x), bf_lo(zw.y), bf_hi(zw.y)}, g = *(const GAS f32x4*)(F.ln1_g + col), b = *(const GAS f32x4*)(F.ln1_b + col);
;             f32x4 a = ((zv - mean1) * rstd1 * g + b) * ALPHA;
; #pragma unroll
;             for (int k = 0; k < 4; ++k) { const int w = *(const GAS int*)(yr + ro[k] + col); const f32x2 lo = __builtin_amdgcn_cvt_pk_f32_fp8(w, false), hi = __builtin_amdgcn_cvt_pk_f32_fp8(w, true); const float g = gk[k] * (1.f / 32.f);
;                 a[0] += g * lo.x; a[1] += g * lo.y; a[2] += g * hi.x; a[3] += g * hi.y; }
	v_ashrrev_i32_e32 v33, 31, v32
	v_lshlrev_b32_e32 v186, 16, v133
	v_and_b32_e32 v187, 0xffff0000, v133
	v_pk_fma_f32 v[0:1], v[0:1], v[118:119], v[12:13]
	v_pk_fma_f32 v[12:13], v[20:21], v[130:131], v[24:25]
	v_pk_fma_f32 v[20:21], v[48:49], v[162:163], v[52:53]
	v_lshlrev_b64 v[48:49], 11, v[154:155]
	v_lshlrev_b64 v[32:33], 19, v[32:33]
	v_lshlrev_b32_e32 v184, 16, v132
	v_and_b32_e32 v185, 0xffff0000, v132
	v_sub_f32_e32 v133, v171, v152
	v_sub_f32_e32 v132, v170, v152
	v_sub_f32_e32 v165, v179, v152
	v_sub_f32_e32 v164, v178, v152
	v_sub_f32_e32 v169, v183, v152
	v_sub_f32_e32 v168, v182, v152
	v_sub_f32_e32 v173, v187, v152
	v_sub_f32_e32 v172, v186, v152
	s_waitcnt lgkmcnt(2)
	v_ashrrev_i32_e32 v35, 31, v34
	s_waitcnt vmcnt(2)
	v_ashrrev_i32_e32 v53, 31, v148
	v_mov_b32_e32 v52, v148
	v_lshl_add_u64 v[32:33], v[48:49], 0, v[32:33]
	v_sub_f32_e32 v167, v181, v152
	v_sub_f32_e32 v166, v180, v152
	v_pk_mul_f32 v[120:121], v[152:153], v[120:121] op_sel:[1,0]
	v_pk_mul_f32 v[132:133], v[152:153], v[132:133] op_sel:[1,0]
	v_pk_mul_f32 v[164:165], v[152:153], v[164:165] op_sel:[1,0]
	v_pk_mul_f32 v[168:169], v[152:153], v[168:169] op_sel:[1,0]
	v_pk_mul_f32 v[172:173], v[152:153], v[172:173] op_sel:[1,0]
	v_lshlrev_b64 v[34:35], 19, v[34:35]
	v_lshlrev_b64 v[48:49], 11, v[52:53]
	v_lshl_add_u64 v[32:33], v[72:73], 0, v[32:33]
	v_pk_mul_f32 v[166:167], v[152:153], v[166:167] op_sel:[1,0]
	v_pk_fma_f32 v[2:3], v[2:3], v[120:121], v[14:15]
	v_pk_fma_f32 v[14:15], v[22:23], v[132:133], v[26:27]
	v_pk_fma_f32 v[22:23], v[50:51], v[164:165], v[54:55]
	v_pk_fma_f32 v[26:27], v[58:59], v[168:169], v[62:63]
	v_pk_fma_f32 v[30:31], v[66:67], v[172:173], v[70:71]
	v_lshl_add_u64 v[34:35], v[48:49], 0, v[34:35]
	global_load_dword v49, v[32:33], off
	global_load_dword v51, v[32:33], off offset:256
	global_load_dword v58, v[32:33], off offset:512
	global_load_dword v62, v[32:33], off offset:768
	global_load_dword v66, v[32:33], off offset:1024
	global_load_dword v70, v[32:33], off offset:1280
	global_load_dword v120, v[32:33], off offset:1536
	v_pk_fma_f32 v[24:25], v[56:57], v[166:167], v[60:61]
	s_waitcnt lgkmcnt(1)
	v_ashrrev_i32_e32 v41, 31, v40
	s_waitcnt lgkmcnt(0)
	v_ashrrev_i32_e32 v43, 31, v42
	v_ashrrev_i32_e32 v55, 31, v149
	v_mov_b32_e32 v54, v149
	v_ashrrev_i32_e32 v57, 31, v150
	v_mov_b32_e32 v56, v150
	v_lshlrev_b64 v[40:41], 19, v[40:41]
	v_lshlrev_b64 v[42:43], 19, v[42:43]
	v_lshlrev_b64 v[52:53], 11, v[54:55]
	v_lshlrev_b64 v[54:55], 11, v[56:57]
	v_sub_f32_e32 v171, v185, v152
	v_sub_f32_e32 v170, v184, v152
	v_lshl_add_u64 v[40:41], v[52:53], 0, v[40:41]
	v_lshl_add_u64 v[42:43], v[54:55], 0, v[42:43]
	v_lshl_add_u64 v[34:35], v[72:73], 0, v[34:35]
	v_pk_mul_f32 v[152:153], v[152:153], v[170:171] op_sel:[1,0]
	v_mul_f32_e32 v50, 0x3d000000, v143
	v_lshl_add_u64 v[40:41], v[72:73], 0, v[40:41]
	v_lshl_add_u64 v[42:43], v[72:73], 0, v[42:43]
	global_load_dword v124, v[34:35], off
	global_load_dword v128, v[40:41], off
	global_load_dword v132, v[42:43], off
	global_load_dword v143, v[34:35], off offset:256
	global_load_dword v150, v[40:41], off offset:256
	global_load_dword v154, v[42:43], off offset:256
	global_load_dword v158, v[34:35], off offset:512
	global_load_dword v162, v[40:41], off offset:512
	global_load_dword v166, v[42:43], off offset:512
	global_load_dword v170, v[34:35], off offset:768
	global_load_dword v174, v[40:41], off offset:768
	global_load_dword v178, v[42:43], off offset:768
	global_load_dword v182, v[34:35], off offset:1024
	global_load_dword v186, v[40:41], off offset:1024
	global_load_dword v190, v[42:43], off offset:1024
	global_load_dword v194, v[34:35], off offset:1280
	global_load_dword v198, v[40:41], off offset:1280
	global_load_dword v202, v[42:43], off offset:1280
	global_load_dword v206, v[34:35], off offset:1536
	global_load_dword v210, v[40:41], off offset:1536
	global_load_dword v214, v[42:43], off offset:1536
	s_nop 0
	global_load_dword v33, v[32:33], off offset:1792
	s_nop 0
	global_load_dword v35, v[34:35], off offset:1792
	s_nop 0
	global_load_dword v226, v[40:41], off offset:1792
	global_load_dword v230, v[42:43], off offset:1792
	v_pk_fma_f32 v[28:29], v[64:65], v[152:153], v[68:69]
	s_waitcnt vmcnt(33)
	v_mul_f32_e32 v48, 0x3d000000, v151
	s_waitcnt vmcnt(32)
	v_mul_f32_e32 v32, 0x3d000000, v156
	v_mul_f32_e32 v34, 0x3d000000, v157
	v_pk_mul_f32 v[2:3], v[2:3], s[12:13] op_sel_hi:[1,0]
	v_pk_mul_f32 v[0:1], v[0:1], s[12:13] op_sel_hi:[1,0]
	v_pk_mul_f32 v[6:7], v[6:7], s[12:13] op_sel_hi:[1,0]
	v_pk_mul_f32 v[4:5], v[4:5], s[12:13] op_sel_hi:[1,0]
	v_pk_mul_f32 v[10:11], v[10:11], s[12:13] op_sel_hi:[1,0]
	v_pk_mul_f32 v[8:9], v[8:9], s[12:13] op_sel_hi:[1,0]
	v_pk_mul_f32 v[14:15], v[14:15], s[12:13] op_sel_hi:[1,0]
	v_pk_mul_f32 v[12:13], v[12:13], s[12:13] op_sel_hi:[1,0]
	v_pk_mul_f32 v[18:19], v[18:19], s[12:13] op_sel_hi:[1,0]
	v_pk_mul_f32 v[16:17], v[16:17], s[12:13] op_sel_hi:[1,0]
	v_pk_mul_f32 v[20:21], v[20:21], s[12:13] op_sel_hi:[1,0]
	v_pk_mul_f32 v[22:23], v[22:23], s[12:13] op_sel_hi:[1,0]
	v_pk_mul_f32 v[26:27], v[26:27], s[12:13] op_sel_hi:[1,0]
	v_pk_mul_f32 v[24:25], v[24:25], s[12:13] op_sel_hi:[1,0]
	v_pk_mul_f32 v[30:31], v[30:31], s[12:13] op_sel_hi:[1,0]
	v_pk_mul_f32 v[28:29], v[28:29], s[12:13] op_sel_hi:[1,0]
	s_waitcnt vmcnt(31)
	v_cvt_pk_f32_fp8_e32 v[40:41], v49
	v_cvt_pk_f32_fp8_sdwa v[42:43], v49 src0_sel:WORD_1
	s_waitcnt vmcnt(30)
	v_cvt_pk_f32_fp8_e32 v[52:53], v51
	v_cvt_pk_f32_fp8_sdwa v[54:55], v51 src0_sel:WORD_1
	s_waitcnt vmcnt(29)
	v_cvt_pk_f32_fp8_e32 v[56:57], v58
	v_cvt_pk_f32_fp8_sdwa v[58:59], v58 src0_sel:WORD_1
	s_waitcnt vmcnt(28)
; #define GAS __attribute__((address_space(1)))
; __device__ __forceinline__ void p9_combine(Frame& F, const LAS int* tstart) {
;     ...
; #pragma unroll
;             for (int k = 0; k < 4; ++k) { const int w = *(const GAS int*)(yr + ro[k] + col); const f32x2 lo = __builtin_amdgcn_cvt_pk_f32_fp8(w, false), hi = __builtin_amdgcn_cvt_pk_f32_fp8(w, true); const float g = gk[k] * (1.f / 32.f);
;                 a[0] += g * lo.x; a[1] += g * lo.y; a[2] += g * hi.x; a[3] += g * hi.y; }
;             v[j] = a; s += (a[0] + a[1]) + (a[2] + a[3]); }
	v_cvt_pk_f32_fp8_e32 v[60:61], v62
	v_cvt_pk_f32_fp8_sdwa v[62:63], v62 src0_sel:WORD_1
	s_waitcnt vmcnt(27)
	v_cvt_pk_f32_fp8_e32 v[64:65], v66
	v_cvt_pk_f32_fp8_sdwa v[66:67], v66 src0_sel:WORD_1
	s_waitcnt vmcnt(26)
	v_cvt_pk_f32_fp8_e32 v[68:69], v70
	s_waitcnt vmcnt(24)
	v_cvt_pk_f32_fp8_e32 v[122:123], v124
	v_cvt_pk_f32_fp8_sdwa v[124:125], v124 src0_sel:WORD_1
	s_waitcnt vmcnt(21)
	v_cvt_pk_f32_fp8_e32 v[144:145], v143
	v_cvt_pk_f32_fp8_sdwa v[146:147], v143 src0_sel:WORD_1
	v_cvt_pk_f32_fp8_sdwa v[70:71], v70 src0_sel:WORD_1
	v_cvt_pk_f32_fp8_e32 v[118:119], v120
	v_cvt_pk_f32_fp8_sdwa v[120:121], v120 src0_sel:WORD_1
	v_cvt_pk_f32_fp8_e32 v[126:127], v128
	v_cvt_pk_f32_fp8_sdwa v[128:129], v128 src0_sel:WORD_1
	s_waitcnt vmcnt(20)
	v_cvt_pk_f32_fp8_e32 v[148:149], v150
	v_cvt_pk_f32_fp8_sdwa v[150:151], v150 src0_sel:WORD_1
	s_waitcnt vmcnt(18)
	v_cvt_pk_f32_fp8_e32 v[156:157], v158
	v_cvt_pk_f32_fp8_sdwa v[158:159], v158 src0_sel:WORD_1
	s_waitcnt vmcnt(15)
	v_cvt_pk_f32_fp8_e32 v[168:169], v170
	v_cvt_pk_f32_fp8_sdwa v[170:171], v170 src0_sel:WORD_1
	s_waitcnt vmcnt(12)
	v_cvt_pk_f32_fp8_e32 v[180:181], v182
	v_cvt_pk_f32_fp8_sdwa v[182:183], v182 src0_sel:WORD_1
	s_waitcnt vmcnt(9)
	v_cvt_pk_f32_fp8_e32 v[192:193], v194
	s_waitcnt vmcnt(3)
	v_cvt_pk_f32_fp8_e32 v[216:217], v33
	v_cvt_pk_f32_fp8_sdwa v[218:219], v33 src0_sel:WORD_1
	v_cvt_pk_f32_fp8_e32 v[130:131], v132
	v_cvt_pk_f32_fp8_sdwa v[132:133], v132 src0_sel:WORD_1
	v_cvt_pk_f32_fp8_e32 v[152:153], v154
	v_cvt_pk_f32_fp8_sdwa v[154:155], v154 src0_sel:WORD_1
	v_cvt_pk_f32_fp8_e32 v[160:161], v162
	v_cvt_pk_f32_fp8_sdwa v[162:163], v162 src0_sel:WORD_1
	v_cvt_pk_f32_fp8_e32 v[172:173], v174
	v_cvt_pk_f32_fp8_sdwa v[174:175], v174 src0_sel:WORD_1
	v_cvt_pk_f32_fp8_e32 v[184:185], v186
	v_cvt_pk_f32_fp8_sdwa v[186:187], v186 src0_sel:WORD_1
	v_cvt_pk_f32_fp8_sdwa v[194:195], v194 src0_sel:WORD_1
	v_cvt_pk_f32_fp8_e32 v[196:197], v198
	v_cvt_pk_f32_fp8_e32 v[204:205], v206
	v_cvt_pk_f32_fp8_sdwa v[206:207], v206 src0_sel:WORD_1
	s_waitcnt vmcnt(2)
	v_cvt_pk_f32_fp8_e32 v[220:221], v35
	v_cvt_pk_f32_fp8_sdwa v[222:223], v35 src0_sel:WORD_1
	v_cvt_pk_f32_fp8_e32 v[164:165], v166
	v_cvt_pk_f32_fp8_sdwa v[166:167], v166 src0_sel:WORD_1
	v_cvt_pk_f32_fp8_e32 v[176:177], v178
	v_cvt_pk_f32_fp8_sdwa v[178:179], v178 src0_sel:WORD_1
	v_cvt_pk_f32_fp8_e32 v[188:189], v190
	v_cvt_pk_f32_fp8_sdwa v[190:191], v190 src0_sel:WORD_1
	v_cvt_pk_f32_fp8_sdwa v[198:199], v198 src0_sel:WORD_1
	v_cvt_pk_f32_fp8_e32 v[200:201], v202
	v_cvt_pk_f32_fp8_e32 v[208:209], v210
	v_pk_fma_f32 v[0:1], v[50:51], v[40:41], v[0:1] op_sel_hi:[0,1,1]
	v_pk_fma_f32 v[2:3], v[50:51], v[42:43], v[2:3] op_sel_hi:[0,1,1]
	v_pk_fma_f32 v[4:5], v[50:51], v[52:53], v[4:5] op_sel_hi:[0,1,1]
	v_pk_fma_f32 v[6:7], v[50:51], v[54:55], v[6:7] op_sel_hi:[0,1,1]
	v_cvt_pk_f32_fp8_sdwa v[202:203], v202 src0_sel:WORD_1
	v_cvt_pk_f32_fp8_e32 v[212:213], v214
	v_pk_fma_f32 v[8:9], v[50:51], v[56:57], v[8:9] op_sel_hi:[0,1,1]
	v_pk_fma_f32 v[10:11], v[50:51], v[58:59], v[10:11] op_sel_hi:[0,1,1]
	v_pk_fma_f32 v[12:13], v[50:51], v[60:61], v[12:13] op_sel_hi:[0,1,1]
	v_pk_fma_f32 v[14:15], v[50:51], v[62:63], v[14:15] op_sel_hi:[0,1,1]
	v_pk_fma_f32 v[16:17], v[50:51], v[64:65], v[16:17] op_sel_hi:[0,1,1]
	v_pk_fma_f32 v[18:19], v[50:51], v[66:67], v[18:19] op_sel_hi:[0,1,1]
	v_pk_fma_f32 v[20:21], v[50:51], v[68:69], v[20:21] op_sel_hi:[0,1,1]
	v_pk_fma_f32 v[0:1], v[48:49], v[122:123], v[0:1] op_sel_hi:[0,1,1]
	v_pk_fma_f32 v[2:3], v[48:49], v[124:125], v[2:3] op_sel_hi:[0,1,1]
	v_pk_fma_f32 v[4:5], v[48:49], v[144:145], v[4:5] op_sel_hi:[0,1,1]
	v_pk_fma_f32 v[6:7], v[48:49], v[146:147], v[6:7] op_sel_hi:[0,1,1]
	v_cvt_pk_f32_fp8_sdwa v[210:211], v210 src0_sel:WORD_1
	v_pk_fma_f32 v[22:23], v[50:51], v[70:71], v[22:23] op_sel_hi:[0,1,1]
	v_pk_fma_f32 v[24:25], v[50:51], v[118:119], v[24:25] op_sel_hi:[0,1,1]
	v_pk_fma_f32 v[26:27], v[50:51], v[120:121], v[26:27] op_sel_hi:[0,1,1]
	v_pk_fma_f32 v[8:9], v[48:49], v[156:157], v[8:9] op_sel_hi:[0,1,1]
	v_pk_fma_f32 v[10:11], v[48:49], v[158:159], v[10:11] op_sel_hi:[0,1,1]
	v_pk_fma_f32 v[12:13], v[48:49], v[168:169], v[12:13] op_sel_hi:[0,1,1]
	v_pk_fma_f32 v[14:15], v[48:49], v[170:171], v[14:15] op_sel_hi:[0,1,1]
	v_pk_fma_f32 v[16:17], v[48:49], v[180:181], v[16:17] op_sel_hi:[0,1,1]
	v_pk_fma_f32 v[18:19], v[48:49], v[182:183], v[18:19] op_sel_hi:[0,1,1]
	v_pk_fma_f32 v[20:21], v[48:49], v[192:193], v[20:21] op_sel_hi:[0,1,1]
	v_pk_fma_f32 v[28:29], v[50:51], v[216:217], v[28:29] op_sel_hi:[0,1,1]
	v_pk_fma_f32 v[30:31], v[50:51], v[218:219], v[30:31] op_sel_hi:[0,1,1]
	v_pk_fma_f32 v[0:1], v[32:33], v[126:127], v[0:1] op_sel_hi:[0,1,1]
	v_pk_fma_f32 v[2:3], v[32:33], v[128:129], v[2:3] op_sel_hi:[0,1,1]
	v_pk_fma_f32 v[4:5], v[32:33], v[148:149], v[4:5] op_sel_hi:[0,1,1]
	v_pk_fma_f32 v[6:7], v[32:33], v[150:151], v[6:7] op_sel_hi:[0,1,1]
	v_cvt_pk_f32_fp8_sdwa v[214:215], v214 src0_sel:WORD_1
	s_waitcnt vmcnt(1)
; #define GAS __attribute__((address_space(1)))
; __device__ __forceinline__ void p9_combine(Frame& F, const LAS int* tstart) {
;     ...
;             for (int k = 0; k < 4; ++k) { const int w = *(const GAS int*)(yr + ro[k] + col); const f32x2 lo = __builtin_amdgcn_cvt_pk_f32_fp8(w, false), hi = __builtin_amdgcn_cvt_pk_f32_fp8(w, true); const float g = gk[k] * (1.f / 32.f);
;                 a[0] += g * lo.x; a[1] += g * lo.y; a[2] += g * hi.x; a[3] += g * hi.y; }
;             v[j] = a; s += (a[0] + a[1]) + (a[2] + a[3]); }
;         const float mean = wave_sum(s) * (1.f / D); float s2 = 0.f;
; #pragma unroll
;         for (int j = 0; j < 8; ++j) { v[j] = v[j] - mean; s2 += (v[j][0] * v[j][0] + v[j][1] * v[j][1]) + (v[j][2] * v[j][2] + v[j][3] * v[j][3]); }
;         const float rstd = 1.f / sqrtf(wave_sum(s2) * (1.f / D) + LN_EPS);
; #pragma unroll
;         for (int j = 0; j < 8; ++j) { const int col = 4 * lane + 256 * j; const f32x4 g = *(const GAS f32x4*)(F.ln2_g + col), b = *(const GAS f32x4*)(F.ln2_b + col);
	v_cvt_pk_f32_fp8_e32 v[224:225], v226
	v_pk_fma_f32 v[22:23], v[48:49], v[194:195], v[22:23] op_sel_hi:[0,1,1]
	v_pk_fma_f32 v[24:25], v[48:49], v[204:205], v[24:25] op_sel_hi:[0,1,1]
	v_pk_fma_f32 v[26:27], v[48:49], v[206:207], v[26:27] op_sel_hi:[0,1,1]
	v_pk_fma_f32 v[8:9], v[32:33], v[160:161], v[8:9] op_sel_hi:[0,1,1]
	v_pk_fma_f32 v[10:11], v[32:33], v[162:163], v[10:11] op_sel_hi:[0,1,1]
	v_pk_fma_f32 v[12:13], v[32:33], v[172:173], v[12:13] op_sel_hi:[0,1,1]
	v_pk_fma_f32 v[14:15], v[32:33], v[174:175], v[14:15] op_sel_hi:[0,1,1]
	v_pk_fma_f32 v[16:17], v[32:33], v[184:185], v[16:17] op_sel_hi:[0,1,1]
	v_pk_fma_f32 v[18:19], v[32:33], v[186:187], v[18:19] op_sel_hi:[0,1,1]
	v_pk_fma_f32 v[20:21], v[32:33], v[196:197], v[20:21] op_sel_hi:[0,1,1]
	v_pk_fma_f32 v[28:29], v[48:49], v[220:221], v[28:29] op_sel_hi:[0,1,1]
	v_pk_fma_f32 v[30:31], v[48:49], v[222:223], v[30:31] op_sel_hi:[0,1,1]
	v_pk_fma_f32 v[40:41], v[34:35], v[130:131], v[0:1] op_sel_hi:[0,1,1]
	v_pk_fma_f32 v[42:43], v[34:35], v[132:133], v[2:3] op_sel_hi:[0,1,1]
	v_pk_fma_f32 v[48:49], v[34:35], v[152:153], v[4:5] op_sel_hi:[0,1,1]
	v_pk_fma_f32 v[50:51], v[34:35], v[154:155], v[6:7] op_sel_hi:[0,1,1]
	v_cvt_pk_f32_fp8_sdwa v[226:227], v226 src0_sel:WORD_1
	v_pk_fma_f32 v[22:23], v[32:33], v[198:199], v[22:23] op_sel_hi:[0,1,1]
	v_pk_fma_f32 v[24:25], v[32:33], v[208:209], v[24:25] op_sel_hi:[0,1,1]
	v_pk_fma_f32 v[52:53], v[34:35], v[164:165], v[8:9] op_sel_hi:[0,1,1]
	v_pk_fma_f32 v[54:55], v[34:35], v[166:167], v[10:11] op_sel_hi:[0,1,1]
	v_pk_fma_f32 v[56:57], v[34:35], v[176:177], v[12:13] op_sel_hi:[0,1,1]
	v_pk_fma_f32 v[58:59], v[34:35], v[178:179], v[14:15] op_sel_hi:[0,1,1]
	v_pk_fma_f32 v[12:13], v[34:35], v[188:189], v[16:17] op_sel_hi:[0,1,1]
	v_pk_fma_f32 v[60:61], v[34:35], v[190:191], v[18:19] op_sel_hi:[0,1,1]
	v_pk_fma_f32 v[8:9], v[34:35], v[200:201], v[20:21] op_sel_hi:[0,1,1]
	v_mov_b32_e32 v14, v40
	v_mov_b32_e32 v15, v48
	v_mov_b32_e32 v16, v41
	v_mov_b32_e32 v17, v49
	v_mov_b32_e32 v18, v42
	v_mov_b32_e32 v19, v50
	v_mov_b32_e32 v20, v43
	v_mov_b32_e32 v21, v51
	v_pk_fma_f32 v[10:11], v[34:35], v[202:203], v[22:23] op_sel_hi:[0,1,1]
	v_pk_fma_f32 v[4:5], v[34:35], v[212:213], v[24:25] op_sel_hi:[0,1,1]
	v_mov_b32_e32 v22, v52
	v_mov_b32_e32 v23, v54
	v_mov_b32_e32 v24, v53
	v_mov_b32_e32 v25, v55
	v_pk_add_f32 v[14:15], v[14:15], v[16:17]
	v_pk_add_f32 v[16:17], v[18:19], v[20:21]
	v_pk_fma_f32 v[26:27], v[32:33], v[210:211], v[26:27] op_sel_hi:[0,1,1]
	v_pk_add_f32 v[18:19], v[22:23], v[24:25]
	v_pk_add_f32 v[14:15], v[14:15], v[16:17]
	s_waitcnt vmcnt(0)
	v_cvt_pk_f32_fp8_e32 v[228:229], v230
	v_cvt_pk_f32_fp8_sdwa v[230:231], v230 src0_sel:WORD_1
	v_pk_fma_f32 v[6:7], v[34:35], v[214:215], v[26:27] op_sel_hi:[0,1,1]
	v_pk_fma_f32 v[0:1], v[32:33], v[224:225], v[28:29] op_sel_hi:[0,1,1]
	v_pk_add_f32 v[26:27], v[56:57], v[56:57] op_sel:[0,1] op_sel_hi:[1,0]
	v_pk_add_f32 v[28:29], v[58:59], v[58:59] op_sel:[0,1] op_sel_hi:[1,0]
	v_pk_add_f32 v[16:17], v[18:19], v[18:19] op_sel:[0,1] op_sel_hi:[1,0]
	v_add_f32_e32 v14, 0, v14
	v_pk_fma_f32 v[2:3], v[32:33], v[226:227], v[30:31] op_sel_hi:[0,1,1]
	v_mov_b32_e32 v31, v12
	v_mov_b32_e32 v27, v60
	v_mov_b32_e32 v29, v61
	v_mov_b32_e32 v17, v13
	v_add_f32_e32 v30, v14, v15
	v_mov_b32_e32 v32, v8
	v_mov_b32_e32 v33, v10
	v_mov_b32_e32 v62, v9
	v_mov_b32_e32 v63, v11
	v_pk_add_f32 v[18:19], v[26:27], v[28:29]
	v_pk_add_f32 v[14:15], v[30:31], v[16:17]
	v_pk_add_f32 v[20:21], v[32:33], v[62:63]
	v_pk_add_f32 v[14:15], v[14:15], v[18:19]
	v_pk_add_f32 v[64:65], v[4:5], v[4:5] op_sel:[0,1] op_sel_hi:[1,0]
	v_pk_add_f32 v[66:67], v[6:7], v[6:7] op_sel:[0,1] op_sel_hi:[1,0]
	v_pk_fma_f32 v[0:1], v[34:35], v[228:229], v[0:1] op_sel_hi:[0,1,1]
	v_pk_fma_f32 v[2:3], v[34:35], v[230:231], v[2:3] op_sel_hi:[0,1,1]
	v_pk_add_f32 v[20:21], v[20:21], v[20:21] op_sel:[0,1] op_sel_hi:[1,0]
	v_pk_add_f32 v[14:15], v[14:15], v[14:15] op_sel:[0,1] op_sel_hi:[1,0]
	v_mov_b32_e32 v65, v2
	v_mov_b32_e32 v67, v3
	v_mov_b32_e32 v21, v1
	v_mov_b32_e32 v15, v0
	v_pk_add_f32 v[22:23], v[64:65], v[66:67]
	v_pk_add_f32 v[14:15], v[14:15], v[20:21]
	s_nop 0
	v_pk_add_f32 v[14:15], v[14:15], v[22:23]
	s_nop 0
	v_add_f32_e32 v14, v14, v15
	global_load_dwordx4 v[144:147], v[94:95], off offset:1024
	global_load_dwordx4 v[148:151], v[96:97], off offset:1024
	global_load_dwordx4 v[152:155], v[94:95], off offset:2048
	global_load_dwordx4 v[156:159], v[96:97], off offset:2048
	global_load_dwordx4 v[160:163], v[94:95], off offset:3072
	global_load_dwordx4 v[164:167], v[96:97], off offset:3072
	global_load_dwordx4 v[168:171], v[98:99], off
	global_load_dwordx4 v[172:175], v[100:101], off
	global_load_dwordx4 v[176:179], v[102:103], off
	global_load_dwordx4 v[180:183], v[104:105], off
	global_load_dwordx4 v[184:187], v[106:107], off
	global_load_dwordx4 v[188:191], v[108:109], off
	global_load_dwordx4 v[192:195], v[110:111], off
	global_load_dwordx4 v[196:199], v[112:113], off
	s_waitcnt lgkmcnt(0)
	s_nop 1
	v_add_f32_dpp v14, v14, v14 quad_perm:[1,0,3,2] row_mask:0xf bank_mask:0xf
	s_waitcnt lgkmcnt(0)
	s_nop 1
	v_add_f32_dpp v14, v14, v14 quad_perm:[2,3,0,1] row_mask:0xf bank_mask:0xf
	s_waitcnt lgkmcnt(0)
	s_nop 1
	v_add_f32_dpp v14, v14, v14 row_half_mirror row_mask:0xf bank_mask:0xf
	s_waitcnt lgkmcnt(0)
	s_nop 1
	v_add_f32_dpp v14, v14, v14 row_mirror row_mask:0xf bank_mask:0xf
	s_waitcnt lgkmcnt(0)
	v_mov_b32_e32 v15, v14
	s_nop 1
	v_permlane16_swap_b32_e32 v14, v15
	v_add_f32_e32 v14, v14, v15
	s_waitcnt lgkmcnt(0)
; __device__ __forceinline__ void p9_combine(Frame& F, const LAS int* tstart) {
;     ...
;         const float mean = wave_sum(s) * (1.f / D); float s2 = 0.f;
; #pragma unroll
;         for (int j = 0; j < 8; ++j) { v[j] = v[j] - mean; s2 += (v[j][0] * v[j][0] + v[j][1] * v[j][1]) + (v[j][2] * v[j][2] + v[j][3] * v[j][3]); }
;         const float rstd = 1.f / sqrtf(wave_sum(s2) * (1.f / D) + LN_EPS);
	v_mov_b32_e32 v15, v14
	s_nop 1
	v_permlane32_swap_b32_e32 v14, v15
	v_add_f32_e32 v14, v14, v15
	v_fmamk_f32 v43, v14, 0xba000000, v43
	v_fmamk_f32 v41, v14, 0xba000000, v41
	v_fmamk_f32 v51, v14, 0xba000000, v51
	v_fmamk_f32 v49, v14, 0xba000000, v49
	v_fmac_f32_e32 v42, 0xba000000, v14
	v_fmac_f32_e32 v40, 0xba000000, v14
	v_fmac_f32_e32 v50, 0xba000000, v14
	v_fmac_f32_e32 v48, 0xba000000, v14
	v_fmamk_f32 v53, v14, 0xba000000, v53
	v_fmac_f32_e32 v52, 0xba000000, v14
	v_fmamk_f32 v55, v14, 0xba000000, v55
	v_fmac_f32_e32 v54, 0xba000000, v14
	v_mov_b32_e32 v16, v41
	v_mov_b32_e32 v17, v49
	v_mov_b32_e32 v20, v43
	v_mov_b32_e32 v21, v51
	v_fmamk_f32 v57, v14, 0xba000000, v57
	v_fmac_f32_e32 v56, 0xba000000, v14
	v_fmamk_f32 v59, v14, 0xba000000, v59
	v_fmac_f32_e32 v58, 0xba000000, v14
	v_fmamk_f32 v61, v14, 0xba000000, v61
	v_fmac_f32_e32 v60, 0xba000000, v14
	v_fmamk_f32 v13, v14, 0xba000000, v13
	v_fmac_f32_e32 v12, 0xba000000, v14
	v_fmamk_f32 v9, v14, 0xba000000, v9
	v_fmac_f32_e32 v8, 0xba000000, v14
	v_fmamk_f32 v11, v14, 0xba000000, v11
	v_fmac_f32_e32 v10, 0xba000000, v14
	v_fmamk_f32 v5, v14, 0xba000000, v5
	v_fmac_f32_e32 v4, 0xba000000, v14
	v_fmamk_f32 v7, v14, 0xba000000, v7
	v_fmac_f32_e32 v6, 0xba000000, v14
	v_fmamk_f32 v3, v14, 0xba000000, v3
	v_fmac_f32_e32 v2, 0xba000000, v14
	v_fmamk_f32 v1, v14, 0xba000000, v1
	v_fmac_f32_e32 v0, 0xba000000, v14
	v_mov_b32_e32 v14, v40
	v_mov_b32_e32 v15, v48
	v_mov_b32_e32 v18, v42
	v_mov_b32_e32 v19, v50
	v_pk_mul_f32 v[22:23], v[54:55], v[54:55]
	v_pk_mul_f32 v[24:25], v[52:53], v[52:53]
	v_pk_mul_f32 v[16:17], v[16:17], v[16:17]
	v_pk_mul_f32 v[20:21], v[20:21], v[20:21]
	v_pk_mov_b32 v[64:65], v[24:25], v[22:23] op_sel:[1,0]
	v_mov_b32_e32 v25, v23
	v_pk_fma_f32 v[14:15], v[14:15], v[14:15], v[16:17]
	v_pk_fma_f32 v[16:17], v[18:19], v[18:19], v[20:21]
	v_mul_f32_e32 v26, v56, v56
	v_mul_f32_e32 v28, v58, v58
	v_pk_add_f32 v[18:19], v[64:65], v[24:25]
	v_pk_add_f32 v[14:15], v[14:15], v[16:17]
	v_pk_fma_f32 v[22:23], v[56:57], v[56:57], v[26:27] op_sel_hi:[1,1,0]
	v_pk_fma_f32 v[26:27], v[58:59], v[58:59], v[28:29] op_sel_hi:[1,1,0]
	v_pk_add_f32 v[16:17], v[18:19], v[18:19] op_sel_hi:[0,1]
	v_pk_add_f32 v[14:15], v[14:15], v[14:15] op_sel_hi:[0,1]
	v_pk_mul_f32 v[30:31], v[10:11], v[10:11]
	v_pk_mul_f32 v[32:33], v[8:9], v[8:9]
	v_mul_f32_e32 v22, v12, v12
	v_mul_f32_e32 v26, v13, v13
	v_mul_f32_e32 v16, v60, v60
	v_mul_f32_e32 v14, v61, v61
	v_pk_mov_b32 v[28:29], v[32:33], v[30:31] op_sel:[1,0]
	v_mov_b32_e32 v33, v31
	v_pk_add_f32 v[18:19], v[22:23], v[26:27]
	v_pk_add_f32 v[14:15], v[16:17], v[14:15]
	v_mul_f32_e32 v34, v4, v4
	v_mul_f32_e32 v62, v6, v6
	v_pk_add_f32 v[20:21], v[28:29], v[32:33]
	v_pk_add_f32 v[14:15], v[18:19], v[14:15]
	v_pk_fma_f32 v[30:31], v[4:5], v[4:5], v[34:35] op_sel_hi:[1,1,0]
	v_pk_fma_f32 v[34:35], v[6:7], v[6:7], v[62:63] op_sel_hi:[1,1,0]
	v_pk_add_f32 v[20:21], v[20:21], v[20:21] op_sel_hi:[0,1]
	v_pk_add_f32 v[14:15], v[14:15], v[14:15] op_sel_hi:[0,1]
	v_mul_f32_e32 v30, v0, v0
	v_mul_f32_e32 v34, v1, v1
	v_mul_f32_e32 v20, v2, v2
	v_mul_f32_e32 v14, v3, v3
	v_pk_add_f32 v[22:23], v[30:31], v[34:35]
	v_pk_add_f32 v[14:15], v[20:21], v[14:15]
	s_nop 0
	v_pk_add_f32 v[14:15], v[22:23], v[14:15]
	s_nop 0
	v_add_f32_e32 v14, v14, v15
	s_waitcnt lgkmcnt(0)
	s_nop 1
	v_add_f32_dpp v14, v14, v14 quad_perm:[1,0,3,2] row_mask:0xf bank_mask:0xf
	s_waitcnt lgkmcnt(0)
	s_nop 1
	v_add_f32_dpp v14, v14, v14 quad_perm:[2,3,0,1] row_mask:0xf bank_mask:0xf
	s_waitcnt lgkmcnt(0)
	s_nop 1
	v_add_f32_dpp v14, v14, v14 row_half_mirror row_mask:0xf bank_mask:0xf
	s_waitcnt lgkmcnt(0)
; #define GAS __attribute__((address_space(1)))
; __device__ __forceinline__ void p9_combine(Frame& F, const LAS int* tstart) {
;     ...
;         const float rstd = 1.f / sqrtf(wave_sum(s2) * (1.f / D) + LN_EPS);
; #pragma unroll
;         for (int j = 0; j < 8; ++j) { const int col = 4 * lane + 256 * j; const f32x4 g = *(const GAS f32x4*)(F.ln2_g + col), b = *(const GAS f32x4*)(F.ln2_b + col);
;             *(GAS f32x4*)(F.out + (size_t)m * D + col) = v[j] * rstd * g + b; }
	s_nop 1
	v_add_f32_dpp v14, v14, v14 row_mirror row_mask:0xf bank_mask:0xf
	s_waitcnt lgkmcnt(0)
	v_mov_b32_e32 v15, v14
	s_nop 1
	v_permlane16_swap_b32_e32 v14, v15
	v_add_f32_e32 v14, v14, v15
	s_waitcnt lgkmcnt(0)
	v_mov_b32_e32 v15, v14
	s_nop 1
	v_permlane32_swap_b32_e32 v14, v15
	v_add_f32_e32 v14, v14, v15
	v_fmamk_f32 v14, v14, 0x3a000000, v141
	v_mul_f32_e32 v15, 0x4f800000, v14
	v_cmp_gt_f32_e32 vcc, s15, v14
	s_nop 1
	v_cndmask_b32_e32 v14, v14, v15, vcc
	v_sqrt_f32_e32 v15, v14
	s_nop 0
	v_add_u32_e32 v16, -1, v15
	v_add_u32_e32 v17, 1, v15
	v_fma_f32 v18, -v16, v15, v14
	v_fma_f32 v19, -v17, v15, v14
	v_cmp_ge_f32_e64 s[0:1], 0, v18
	s_nop 1
	v_cndmask_b32_e64 v15, v15, v16, s[0:1]
	v_cmp_lt_f32_e64 s[0:1], 0, v19
	s_nop 1
	v_cndmask_b32_e64 v15, v15, v17, s[0:1]
	v_mul_f32_e32 v16, 0x37800000, v15
	v_cndmask_b32_e32 v15, v15, v16, vcc
	v_cmp_class_f32_e32 vcc, v14, v142
	s_nop 1
	v_cndmask_b32_e32 v14, v15, v14, vcc
	v_div_scale_f32 v15, s[0:1], v14, v14, 1.0
	v_rcp_f32_e32 v17, v15
	v_div_scale_f32 v16, vcc, 1.0, v14, 1.0
	v_fma_f32 v18, -v15, v17, 1.0
	v_fmac_f32_e32 v17, v18, v17
	v_mul_f32_e32 v18, v16, v17
	v_fma_f32 v19, -v15, v18, v16
	v_fmac_f32_e32 v18, v19, v17
	v_fma_f32 v15, -v15, v18, v16
	v_div_fmas_f32 v15, v15, v17, v18
	v_div_fixup_f32 v22, v15, v14, 1.0
	v_pk_mul_f32 v[14:15], v[40:41], v[22:23] op_sel_hi:[1,0]
	v_pk_mul_f32 v[16:17], v[42:43], v[22:23] op_sel_hi:[1,0]
	v_pk_fma_f32 v[14:15], v[36:37], v[14:15], v[44:45]
	v_pk_fma_f32 v[16:17], v[38:39], v[16:17], v[46:47]
	global_store_dwordx4 v[114:115], v[14:17], off offset:-4096
	v_pk_mul_f32 v[24:25], v[50:51], v[22:23] op_sel_hi:[1,0]
	v_pk_mul_f32 v[26:27], v[48:49], v[22:23] op_sel_hi:[1,0]
	v_pk_mul_f32 v[12:13], v[12:13], v[22:23] op_sel_hi:[1,0]
	v_pk_mul_f32 v[10:11], v[10:11], v[22:23] op_sel_hi:[1,0]
	v_pk_mul_f32 v[8:9], v[8:9], v[22:23] op_sel_hi:[1,0]
	v_pk_mul_f32 v[6:7], v[6:7], v[22:23] op_sel_hi:[1,0]
	v_pk_mul_f32 v[4:5], v[4:5], v[22:23] op_sel_hi:[1,0]
	v_pk_mul_f32 v[2:3], v[2:3], v[22:23] op_sel_hi:[1,0]
	v_pk_mul_f32 v[0:1], v[0:1], v[22:23] op_sel_hi:[1,0]
	s_waitcnt vmcnt(1)
	v_pk_fma_f32 v[14:15], v[144:145], v[26:27], v[148:149]
	v_pk_fma_f32 v[16:17], v[146:147], v[24:25], v[150:151]
	global_store_dwordx4 v[114:115], v[14:17], off offset:-3072
	v_pk_mul_f32 v[24:25], v[54:55], v[22:23] op_sel_hi:[1,0]
	v_pk_mul_f32 v[26:27], v[52:53], v[22:23] op_sel_hi:[1,0]
	s_nop 0
	v_pk_fma_f32 v[16:17], v[154:155], v[24:25], v[158:159]
	v_pk_fma_f32 v[14:15], v[152:153], v[26:27], v[156:157]
	global_store_dwordx4 v[114:115], v[14:17], off offset:-2048
	v_pk_mul_f32 v[24:25], v[58:59], v[22:23] op_sel_hi:[1,0]
	v_pk_mul_f32 v[26:27], v[56:57], v[22:23] op_sel_hi:[1,0]
	s_nop 0
	v_pk_fma_f32 v[16:17], v[162:163], v[24:25], v[166:167]
	v_pk_fma_f32 v[14:15], v[160:161], v[26:27], v[164:165]
	global_store_dwordx4 v[114:115], v[14:17], off offset:-1024
	v_pk_mul_f32 v[24:25], v[60:61], v[22:23] op_sel_hi:[1,0]
	s_nop 1
	v_pk_fma_f32 v[12:13], v[168:169], v[12:13], v[172:173]
	v_pk_fma_f32 v[14:15], v[170:171], v[24:25], v[174:175]
	global_store_dwordx4 v[114:115], v[12:15], off
	v_pk_fma_f32 v[8:9], v[176:177], v[8:9], v[180:181]
	v_pk_fma_f32 v[10:11], v[178:179], v[10:11], v[182:183]
	global_store_dwordx4 v[114:115], v[8:11], off offset:1024
	v_pk_fma_f32 v[4:5], v[184:185], v[4:5], v[188:189]
	v_pk_fma_f32 v[6:7], v[186:187], v[6:7], v[190:191]
	global_store_dwordx4 v[114:115], v[4:7], off offset:2048
	v_pk_fma_f32 v[0:1], v[192:193], v[0:1], v[196:197]
	v_pk_fma_f32 v[2:3], v[194:195], v[2:3], v[198:199]
	global_store_dwordx4 v[114:115], v[0:3], off offset:3072
	v_lshl_add_u64 v[114:115], v[114:115], 0, s[4:5]
	s_cbranch_scc1 .LBB0_1798
